# v13 + per-iteration L2 re-touch of codebook fragments 4 iterations ahead
# baseline (speedup 1.0000x reference)
.LBB2_414:
	s_movk_i32 s0, 0xc00
	v_mov_b64_e32 v[26:27], s[42:43]
	v_mul_u32_u24_e32 v28, 0xc00, v154
	v_mad_i64_i32 v[26:27], s[0:1], v62, s0, v[26:27]
	v_or_b32_e32 v28, v28, v98
	v_mov_b32_e32 v99, 0
	v_lshl_add_u64 v[26:27], v[26:27], 0, v[98:99]
	v_or_b32_e32 v29, 0x10000, v28
	global_store_dwordx4 v[26:27], v[22:25], off sc1
	ds_write_b128 v29, v[22:25]
	v_sub_f32_e32 v10, v10, v22
	v_or_b32_e32 v22, v101, v154
	v_sub_f32_e32 v11, v11, v23
	v_add_u32_e32 v23, v22, v102
	v_lshl_or_b32 v23, v23, 4, v103
	ds_write_b32 v23, v10
	v_add_u32_e32 v10, v22, v104
	v_lshl_or_b32 v10, v10, 4, v105
	ds_write_b32 v10, v11
	v_or_b32_e32 v10, v106, v154
	v_add_u32_e32 v10, v10, v107
	v_sub_f32_e32 v12, v12, v24
	v_lshl_or_b32 v10, v10, 4, v108
	ds_write_b32 v10, v12
	v_or_b32_e32 v10, v109, v154
	v_add_u32_e32 v10, v10, v110
	v_sub_f32_e32 v13, v13, v25
	v_lshl_or_b32 v10, v10, 4, v111
	ds_write_b32 v10, v13
	v_add_u32_e32 v10, 0x10400, v28
	ds_write_b128 v10, v[18:21]
	v_sub_f32_e32 v10, v6, v18
	v_sub_f32_e32 v11, v7, v19
	v_pk_add_f32 v[6:7], v[8:9], v[20:21] neg_lo:[0,1] neg_hi:[0,1]
	v_or_b32_e32 v8, v112, v154
	v_add_u32_e32 v9, v8, v113
	v_add_u32_e32 v8, v8, v115
	v_lshl_or_b32 v9, v9, 4, v114
	v_lshl_or_b32 v8, v8, 4, v116
	ds_write_b32 v9, v10
	ds_write_b32 v8, v11
	v_or_b32_e32 v8, v117, v154
	v_add_u32_e32 v8, v8, v118
	v_lshl_or_b32 v8, v8, 4, v119
	ds_write_b32 v8, v6
	v_or_b32_e32 v6, v120, v154
	v_add_u32_e32 v6, v6, v121
	v_lshl_or_b32 v6, v6, 4, v122
	ds_write_b32 v6, v7
	v_add_u32_e32 v6, 0x10800, v28
	ds_write_b128 v6, v[14:17]
	v_or_b32_e32 v6, v123, v154
	v_add_u32_e32 v7, v6, v124
	v_pk_add_f32 v[2:3], v[2:3], v[14:15] neg_lo:[0,1] neg_hi:[0,1]
	v_lshl_or_b32 v7, v7, 4, v125
	ds_write_b32 v7, v2
	v_add_u32_e32 v2, v6, v126
	v_lshl_or_b32 v2, v2, 4, v127
	ds_write_b32 v2, v3
	v_or_b32_e32 v2, v133, v154
	v_add_u32_e32 v2, v2, v134
	v_pk_add_f32 v[4:5], v[4:5], v[16:17] neg_lo:[0,1] neg_hi:[0,1]
	v_lshl_or_b32 v2, v2, 4, v63
	ds_write_b32 v2, v4
	v_or_b32_e32 v2, v135, v154
	v_add_u32_e32 v2, v2, v132
	v_lshl_or_b32 v2, v2, 4, v136
	v_add_lshl_u32 v4, v100, v154, 4
	s_mov_b32 s5, 0
	s_mov_b32 s4, 1.0
	ds_write_b32 v2, v5
	v_mov_b64_e32 v[2:3], s[4:5]
	v_add_u32_e32 v4, 8, v4
	s_waitcnt vmcnt(1)
	v_lshlrev_b32_e32 v40, 9, v150
	ds_write2st64_b64 v4, v[2:3], v[2:3] offset1:64
	v_or_b32_e32 v2, v40, v128
	v_lshlrev_b32_e32 v98, 4, v2
	v_lshl_add_u64 v[100:101], s[40:41], 0, v[98:99]
	s_mov_b64 s[0:1], 0x787000
	v_lshl_add_u64 v[34:35], v[100:101], 0, s[0:1]
	s_mov_b32 s0, 0x788000
	v_add_co_u32_e32 v36, vcc, s0, v100
	global_store_dwordx4 v[26:27], v[18:21], off offset:1024 sc1
	global_store_dwordx4 v[26:27], v[14:17], off offset:2048 sc1
	s_lshr_b32 s59, s33, 4
	s_and_b32 s59, s59, 31
	s_lshl_b32 s59, s59, 15
	s_add_u32 s59, s59, 0x787000
	s_add_u32 s68, s40, s59
	s_addc_u32 s69, s41, 0
	v_lshlrev_b32_e32 v207, 6, v0
	global_load_dword v207, v207, s[68:69]
	s_waitcnt lgkmcnt(0)
	s_barrier
	v_addc_co_u32_e32 v37, vcc, 0, v101, vcc
	global_load_dwordx4 v[2:5], v[34:35], off offset:1024
	global_load_dwordx4 v[10:13], v[34:35], off offset:2048
	global_load_dwordx4 v[14:17], v[34:35], off offset:3072
	global_load_dwordx4 v[6:9], v[36:37], off offset:-4096
	global_load_dwordx4 v[18:21], v[36:37], off
	global_load_dwordx4 v[22:25], v[36:37], off offset:1024
	global_load_dwordx4 v[26:29], v[36:37], off offset:2048
	global_load_dwordx4 v[30:33], v[36:37], off offset:3072
	v_and_b32_e32 v35, 15, v0
	v_lshrrev_b32_e32 v37, 4, v128
	v_lshlrev_b32_e32 v102, 2, v35
	v_lshlrev_b32_e32 v41, 2, v37
	v_lshlrev_b32_e32 v34, 4, v35
	v_cmp_gt_u32_e64 s[0:1], 6, v35
	v_mov_b32_e32 v35, v99
	v_or3_b32 v36, v34, v41, v40
	v_lshl_add_u64 v[104:105], s[44:45], 0, v[34:35]
	v_or_b32_e32 v34, v40, v34
	s_movk_i32 s4, 0x1000
	v_or3_b32 v153, v34, v41, s4
	v_or_b32_e32 v34, 0x11800, v98
	v_lshl_add_u64 v[118:119], s[40:41], 0, v[34:35]
	v_or_b32_e32 v34, 0x11400, v98
	v_lshl_add_u64 v[120:121], s[40:41], 0, v[34:35]
	v_or_b32_e32 v34, 0x11000, v98
	ds_read2st64_b32 v[132:133], v36 offset1:1
	v_or_b32_e32 v36, s33, v41
	v_lshl_add_u64 v[122:123], s[40:41], 0, v[34:35]
	v_or_b32_e32 v34, 0x10c00, v98
	v_or_b32_e32 v38, 1, v36
	v_lshl_add_u64 v[124:125], s[40:41], 0, v[34:35]
	v_or_b32_e32 v34, 0x10800, v98
	v_mul_u32_u24_e32 v152, 0x3000, v37
	v_ashrrev_i32_e32 v37, 31, v36
	v_ashrrev_i32_e32 v39, 31, v38
	v_lshl_add_u64 v[126:127], s[40:41], 0, v[34:35]
	v_or_b32_e32 v34, 0x10400, v98
	v_mov_b32_e32 v103, v99
	v_lshlrev_b64 v[108:109], 17, v[36:37]
	v_lshlrev_b64 v[110:111], 17, v[38:39]
	v_or_b32_e32 v38, 2, v36
	v_or_b32_e32 v36, 3, v36
	v_lshl_add_u64 v[128:129], s[40:41], 0, v[34:35]
	v_mul_u32_u24_e32 v34, 24, v150
	v_lshl_add_u64 v[106:107], s[38:39], 0, v[102:103]
	v_ashrrev_i32_e32 v39, 31, v38
	v_ashrrev_i32_e32 v37, 31, v36
	v_lshlrev_b32_e32 v103, 2, v0
	v_or_b32_e32 v98, 0x11c00, v98
	v_or_b32_e32 v34, v152, v34
	v_lshlrev_b64 v[112:113], 17, v[38:39]
	v_lshlrev_b64 v[114:115], 17, v[36:37]
	v_and_b32_e32 v116, 0x700, v103
	v_mov_b32_e32 v117, v99
	v_lshl_add_u64 v[130:131], s[40:41], 0, v[98:99]
	v_add_u32_e32 v154, v34, v102
	s_mov_b64 s[6:7], 0
	s_mov_b64 s[8:9], 0x800
	v_mov_b32_e32 v155, 0x400
	v_mov_b32_e32 v159, 0
	v_mov_b32_e32 v158, 0
	v_mov_b32_e32 v157, 0
	v_mov_b32_e32 v156, 0
	v_readfirstlane_b32 s78, v150
	v_and_b32_e32 v104, 63, v0
	v_lshlrev_b32_e32 v104, 4, v104
	v_lshl_or_b32 v104, v150, 13, v104
	v_add_u32_e32 v105, 0xfffff000, v153
	v_mov_b32_e32 v106, v154
	v_lshrrev_b32_e32 v98, 2, v102
	v_cmp_gt_u32_e32 vcc, 6, v98
	v_add_u32_e32 v107, -6, v98
	s_nop 0
	v_cndmask_b32_e32 v107, v107, v98, vcc
	v_cmp_gt_u32_e32 vcc, 6, v107
	v_add_u32_e32 v98, -6, v107
	s_nop 0
	v_cndmask_b32_e32 v107, v98, v107, vcc
	v_lshlrev_b32_e32 v107, 2, v107
	v_sub_u32_e32 v106, v106, v102
	v_add_u32_e32 v106, v106, v107
	v_and_b32_e32 v98, 63, v0
	v_lshrrev_b32_e32 v98, 4, v98
	v_lshlrev_b32_e32 v98, 19, v98
	v_lshl_or_b32 v108, v102, 2, v98
	v_add_u32_e32 v109, 0x20000, v108
	v_add_u32_e32 v110, 0x40000, v108
	v_add_u32_e32 v111, 0x60000, v108
	v_mov_b32_e32 v240, 0
	v_mov_b32_e32 v241, 0
	v_mov_b32_e32 v242, 0
	v_mov_b32_e32 v243, 0
	s_lshl_b32 s84, s33, 17
	s_lshl_b32 s85, s78, 10
	s_add_u32 s84, s84, s85
	s_add_u32 s80, s44, s84
	s_addc_u32 s81, s45, 0
	s_mul_i32 s84, s78, 0x1800
	s_add_u32 s94, s38, s84
	s_addc_u32 s95, s39, 0
	s_mov_b32 s70, 0
	v_and_b32_e32 v100, 63, v0
	v_lshlrev_b32_e32 v100, 7, v100
	v_lshl_or_b32 v100, v150, 13, v100
	s_add_u32 s86, s40, 0x797000
	s_addc_u32 s87, s41, 0
	s_add_u32 s88, s86, 0x1000
	s_addc_u32 s89, s87, 0
	v_add_u32_e32 v112, 0x1000, v105
	s_waitcnt vmcnt(0) lgkmcnt(0)
	v_mfma_f32_16x16x4_f32 v[34:37], v132, v6, 0
	v_mfma_f32_16x16x4_f32 v[38:41], v132, v8, 0
	v_mfma_f32_16x16x4_f32 v[34:37], v133, v7, v[34:37]
	v_mfma_f32_16x16x4_f32 v[38:41], v133, v9, v[38:41]
	global_load_dwordx4 v[6:9], v104, s[86:87]
	v_mfma_f32_16x16x4_f32 v[42:45], v132, v2, 0
	v_mfma_f32_16x16x4_f32 v[46:49], v132, v4, 0
	v_mfma_f32_16x16x4_f32 v[42:45], v133, v3, v[42:45]
	v_mfma_f32_16x16x4_f32 v[46:49], v133, v5, v[46:49]
	global_load_dwordx4 v[2:5], v104, s[86:87] offset:1024
	v_mfma_f32_16x16x4_f32 v[50:53], v132, v10, 0
	v_mfma_f32_16x16x4_f32 v[54:57], v132, v12, 0
	v_mfma_f32_16x16x4_f32 v[50:53], v133, v11, v[50:53]
	v_mfma_f32_16x16x4_f32 v[54:57], v133, v13, v[54:57]
	global_load_dwordx4 v[10:13], v104, s[86:87] offset:2048
	v_mfma_f32_16x16x4_f32 v[58:61], v132, v14, 0
	v_mfma_f32_16x16x4_f32 v[62:65], v132, v16, 0
	v_mfma_f32_16x16x4_f32 v[58:61], v133, v15, v[58:61]
	v_mfma_f32_16x16x4_f32 v[62:65], v133, v17, v[62:65]
	global_load_dwordx4 v[14:17], v104, s[86:87] offset:3072
	v_mfma_f32_16x16x4_f32 v[66:69], v132, v18, 0
	v_mfma_f32_16x16x4_f32 v[70:73], v132, v20, 0
	v_mfma_f32_16x16x4_f32 v[66:69], v133, v19, v[66:69]
	v_mfma_f32_16x16x4_f32 v[70:73], v133, v21, v[70:73]
	global_load_dwordx4 v[18:21], v104, s[88:89]
	v_mfma_f32_16x16x4_f32 v[74:77], v132, v22, 0
	v_mfma_f32_16x16x4_f32 v[78:81], v132, v24, 0
	v_mfma_f32_16x16x4_f32 v[74:77], v133, v23, v[74:77]
	v_mfma_f32_16x16x4_f32 v[78:81], v133, v25, v[78:81]
	global_load_dwordx4 v[22:25], v104, s[88:89] offset:1024
	v_mfma_f32_16x16x4_f32 v[82:85], v132, v26, 0
	v_mfma_f32_16x16x4_f32 v[86:89], v132, v28, 0
	v_mfma_f32_16x16x4_f32 v[82:85], v133, v27, v[82:85]
	v_mfma_f32_16x16x4_f32 v[86:89], v133, v29, v[86:89]
	global_load_dwordx4 v[26:29], v104, s[88:89] offset:2048
	v_mfma_f32_16x16x4_f32 v[90:93], v132, v30, 0
	v_mfma_f32_16x16x4_f32 v[94:97], v132, v32, 0
	v_mfma_f32_16x16x4_f32 v[90:93], v133, v31, v[90:93]
	v_mfma_f32_16x16x4_f32 v[94:97], v133, v33, v[94:97]
	global_load_dwordx4 v[30:33], v104, s[88:89] offset:3072
	ds_read2st64_b32 v[132:133], v112 offset1:1
	s_nop 7
	s_nop 7
	v_max3_f32 v114, v34, v38, v42
	v_max3_f32 v116, v46, v50, v54
	v_max3_f32 v114, v114, v58, v62
	v_max3_f32 v116, v116, v66, v70
	v_max3_f32 v114, v114, v74, v78
	v_max3_f32 v116, v116, v82, v86
	v_max3_f32 v114, v114, v90, v94
	v_max_f32_e32 v114, v114, v116
	s_nop 1
	v_max_f32_dpp v114, v114, v114 row_ror:1 row_mask:0xf bank_mask:0xf
	s_nop 1
	v_max_f32_dpp v114, v114, v114 row_ror:2 row_mask:0xf bank_mask:0xf
	s_nop 1
	v_max_f32_dpp v114, v114, v114 row_ror:4 row_mask:0xf bank_mask:0xf
	s_nop 1
	v_max_f32_dpp v114, v114, v114 row_ror:8 row_mask:0xf bank_mask:0xf
	s_waitcnt vmcnt(0) lgkmcnt(0)
.Lk3m_loop:
	s_waitcnt lgkmcnt(0)
	s_lshl_b32 s84, s70, 13
	s_add_u32 s90, s80, s84
	s_addc_u32 s91, s81, 0
	s_mul_i32 s84, s70, 0xc000
	s_add_u32 s92, s94, s84
	s_addc_u32 s93, s95, 0
	s_add_i32 s84, s70, 2
	s_and_b32 s84, s84, 15
	s_lshl_b32 s82, s84, 12
	s_lshl_b32 s84, s84, 16
	s_add_u32 s84, s84, 0x787000
	s_add_u32 s86, s40, s84
	s_addc_u32 s87, s41, 0
	s_add_u32 s88, s86, 0x1000
	s_addc_u32 s89, s87, 0
	s_add_i32 s84, s70, 15
	s_and_b32 s84, s84, 15
	s_mul_i32 s84, s84, 0xc0
	s_add_u32 s83, s84, 0x10000
	v_add_u32_e32 v112, s82, v105
	s_add_i32 s84, s70, 4
	s_and_b32 s84, s84, 15
	s_lshl_b32 s84, s84, 16
	s_add_u32 s84, s84, 0x787000
	s_add_u32 s58, s40, s84
	s_addc_u32 s59, s41, 0
	global_load_dword v98, v100, s[58:59]
	v_sub_f32_e32 v120, v94, v114
	v_cmp_eq_f32_e64 s[72:73], v94, v114
	s_waitcnt vmcnt(28)
	v_mfma_f32_16x16x4_f32 v[176:179], v132, v6, 0
	ds_read2st64_b32 v[254:255], v112 offset1:1
	v_sub_f32_e32 v121, v90, v114
	v_cmp_eq_f32_e64 s[74:75], v90, v114
	v_exp_f32_e32 v149, v120
	v_cndmask_b32_e64 v118, v155, 15, s[72:73]
	v_max3_f32 v115, v35, v39, v43
	v_sub_f32_e32 v120, v86, v114
	v_cmp_eq_f32_e64 s[76:77], v86, v114
	v_exp_f32_e32 v148, v121
	v_cndmask_b32_e64 v118, v118, 14, s[74:75]
	v_mfma_f32_16x16x4_f32 v[180:183], v132, v8, 0
	v_sub_f32_e32 v121, v82, v114
	v_max3_f32 v117, v47, v51, v55
	v_cmp_eq_f32_e64 s[72:73], v82, v114
	v_exp_f32_e32 v147, v120
	v_cndmask_b32_e64 v118, v118, 13, s[76:77]
	v_sub_f32_e32 v120, v78, v114
	v_cmp_eq_f32_e64 s[74:75], v78, v114
	v_max3_f32 v115, v115, v59, v63
	v_exp_f32_e32 v146, v121
	v_cndmask_b32_e64 v118, v118, 12, s[72:73]
	v_mfma_f32_16x16x4_f32 v[176:179], v133, v7, v[176:179]
	v_sub_f32_e32 v121, v74, v114
	v_cmp_eq_f32_e64 s[76:77], v74, v114
	v_exp_f32_e32 v145, v120
	v_cndmask_b32_e64 v118, v118, 11, s[74:75]
	v_max3_f32 v117, v117, v67, v71
	v_sub_f32_e32 v120, v70, v114
	v_cmp_eq_f32_e64 s[72:73], v70, v114
	v_exp_f32_e32 v144, v121
	v_cndmask_b32_e64 v118, v118, 10, s[76:77]
	v_mfma_f32_16x16x4_f32 v[180:183], v133, v9, v[180:183]
	global_load_dwordx4 v[6:9], v104, s[86:87]
	v_sub_f32_e32 v121, v66, v114
	v_max3_f32 v115, v115, v75, v79
	v_cmp_eq_f32_e64 s[74:75], v66, v114
	v_exp_f32_e32 v143, v120
	v_cndmask_b32_e64 v118, v118, 9, s[72:73]
	v_sub_f32_e32 v120, v62, v114
	v_cmp_eq_f32_e64 s[76:77], v62, v114
	v_max3_f32 v117, v117, v83, v87
	v_exp_f32_e32 v142, v121
	v_cndmask_b32_e64 v118, v118, 8, s[74:75]
	s_waitcnt vmcnt(28)
	v_mfma_f32_16x16x4_f32 v[184:187], v132, v2, 0
	v_sub_f32_e32 v121, v58, v114
	v_cmp_eq_f32_e64 s[72:73], v58, v114
	v_exp_f32_e32 v141, v120
	v_cndmask_b32_e64 v118, v118, 7, s[76:77]
	v_max3_f32 v115, v115, v91, v95
	v_sub_f32_e32 v120, v54, v114
	v_cmp_eq_f32_e64 s[74:75], v54, v114
	v_exp_f32_e32 v140, v121
	v_cndmask_b32_e64 v118, v118, 6, s[72:73]
	v_mfma_f32_16x16x4_f32 v[188:191], v132, v4, 0
	v_sub_f32_e32 v121, v50, v114
	v_max_f32_e32 v115, v115, v117
	v_cmp_eq_f32_e64 s[76:77], v50, v114
	v_exp_f32_e32 v139, v120
	v_cndmask_b32_e64 v118, v118, 5, s[74:75]
	v_sub_f32_e32 v120, v46, v114
	v_cmp_eq_f32_e64 s[72:73], v46, v114
	v_max_f32_dpp v115, v115, v115 row_ror:1 row_mask:0xf bank_mask:0xf
	v_exp_f32_e32 v138, v121
	v_cndmask_b32_e64 v118, v118, 4, s[76:77]
	v_mfma_f32_16x16x4_f32 v[184:187], v133, v3, v[184:187]
	v_sub_f32_e32 v121, v42, v114
	v_cmp_eq_f32_e64 s[74:75], v42, v114
	v_exp_f32_e32 v137, v120
	v_cndmask_b32_e64 v118, v118, 3, s[72:73]
	v_max_f32_dpp v115, v115, v115 row_ror:2 row_mask:0xf bank_mask:0xf
	v_sub_f32_e32 v120, v38, v114
	v_cmp_eq_f32_e64 s[76:77], v38, v114
	v_exp_f32_e32 v136, v121
	v_cndmask_b32_e64 v118, v118, 2, s[74:75]
	v_mfma_f32_16x16x4_f32 v[188:191], v133, v5, v[188:191]
	global_load_dwordx4 v[2:5], v104, s[86:87] offset:1024
	v_sub_f32_e32 v121, v34, v114
	v_max_f32_dpp v115, v115, v115 row_ror:4 row_mask:0xf bank_mask:0xf
	v_cmp_eq_f32_e64 s[72:73], v34, v114
	v_exp_f32_e32 v135, v120
	v_cndmask_b32_e64 v118, v118, 1, s[76:77]
	v_exp_f32_e32 v134, v121
	v_cndmask_b32_e64 v118, v118, 0, s[72:73]
	v_max_f32_dpp v115, v115, v115 row_ror:8 row_mask:0xf bank_mask:0xf
	v_sub_f32_e32 v120, v95, v115
	v_cmp_eq_f32_e64 s[72:73], v95, v115
	v_max3_f32 v114, v36, v40, v44
	s_waitcnt vmcnt(28)
	v_mfma_f32_16x16x4_f32 v[192:195], v132, v10, 0
	v_sub_f32_e32 v121, v91, v115
	v_and_b32_e32 v122, 12, v118
	v_cmp_eq_f32_e64 s[74:75], v91, v115
	v_and_b32_e32 v124, 3, v118
	v_exp_f32_e32 v175, v120
	v_add_f32_e32 v128, v134, v135
	v_cndmask_b32_e64 v119, v155, 15, s[72:73]
	v_add_f32_e32 v130, v136, v137
	v_sub_f32_e32 v120, v87, v115
	v_max3_f32 v116, v48, v52, v56
	v_cmp_eq_f32_e64 s[76:77], v87, v115
	v_exp_f32_e32 v174, v121
	v_lshl_or_b32 v122, v122, 4, v124
	v_cndmask_b32_e64 v119, v119, 14, s[74:75]
	v_add_f32_e32 v128, v128, v138
	v_mfma_f32_16x16x4_f32 v[196:199], v132, v12, 0
	v_sub_f32_e32 v121, v83, v115
	v_add_f32_e32 v130, v130, v139
	v_cmp_eq_f32_e64 s[72:73], v83, v115
	v_or_b32_e32 v122, v122, v102
	v_exp_f32_e32 v173, v120
	v_max3_f32 v114, v114, v60, v64
	v_cndmask_b32_e64 v119, v119, 13, s[76:77]
	v_add_f32_e32 v128, v128, v140
	v_sub_f32_e32 v120, v79, v115
	v_cmp_eq_f32_e64 s[74:75], v79, v115
	v_add_f32_e32 v130, v130, v141
	v_exp_f32_e32 v172, v121
	v_max_u32_e32 v126, v122, v118
	v_cndmask_b32_e64 v119, v119, 12, s[72:73]
	v_max3_f32 v116, v116, v68, v72
	v_mfma_f32_16x16x4_f32 v[192:195], v133, v11, v[192:195]
	v_sub_f32_e32 v121, v75, v115
	v_add_f32_e32 v128, v128, v142
	v_cmp_eq_f32_e64 s[76:77], v75, v115
	v_add_f32_e32 v130, v130, v143
	v_exp_f32_e32 v171, v120
	v_min_u32_dpp v126, v126, v126 row_ror:1 row_mask:0xf bank_mask:0xf
	v_cndmask_b32_e64 v119, v119, 11, s[74:75]
	v_sub_f32_e32 v120, v71, v115
	v_add_f32_e32 v128, v128, v144
	v_cmp_eq_f32_e64 s[72:73], v71, v115
	v_max3_f32 v114, v114, v76, v80
	v_exp_f32_e32 v170, v121
	v_add_f32_e32 v130, v130, v145
	v_cndmask_b32_e64 v119, v119, 10, s[76:77]
	v_min_u32_dpp v126, v126, v126 row_ror:2 row_mask:0xf bank_mask:0xf
	v_mfma_f32_16x16x4_f32 v[196:199], v133, v13, v[196:199]
	global_load_dwordx4 v[10:13], v104, s[86:87] offset:2048
	v_sub_f32_e32 v121, v67, v115
	v_add_f32_e32 v128, v128, v146
	v_cmp_eq_f32_e64 s[74:75], v67, v115
	v_max3_f32 v116, v116, v84, v88
	v_exp_f32_e32 v169, v120
	v_cndmask_b32_e64 v119, v119, 9, s[72:73]
	v_add_f32_e32 v130, v130, v147
	v_sub_f32_e32 v120, v63, v115
	v_min_u32_dpp v126, v126, v126 row_ror:4 row_mask:0xf bank_mask:0xf
	v_cmp_eq_f32_e64 s[76:77], v63, v115
	v_add_f32_e32 v128, v128, v148
	v_exp_f32_e32 v168, v121
	v_add_f32_e32 v130, v130, v149
	v_cndmask_b32_e64 v119, v119, 8, s[74:75]
	v_max3_f32 v114, v114, v92, v96
	s_waitcnt vmcnt(25)
	v_mfma_f32_16x16x4_f32 v[200:203], v132, v14, 0
	v_sub_f32_e32 v121, v59, v115
	v_min_u32_dpp v126, v126, v126 row_ror:8 row_mask:0xf bank_mask:0xf
	v_cmp_eq_f32_e64 s[72:73], v59, v115
	v_exp_f32_e32 v167, v120
	v_add_f32_e32 v128, v128, v130
	v_cndmask_b32_e64 v119, v119, 7, s[76:77]
	v_mad_u32_u24 v248, v126, 24, v107
	v_sub_f32_e32 v120, v55, v115
	v_add_f32_dpp v128, v128, v128 row_ror:1 row_mask:0xf bank_mask:0xf
	v_cmp_eq_f32_e64 s[74:75], v55, v115
	v_max_f32_e32 v114, v114, v116
	v_exp_f32_e32 v166, v121
	global_load_dword v240, v248, s[92:93]
	v_cndmask_b32_e64 v119, v119, 6, s[72:73]
	v_add_f32_dpp v128, v128, v128 row_ror:2 row_mask:0xf bank_mask:0xf
	v_mfma_f32_16x16x4_f32 v[204:207], v132, v16, 0
	v_sub_f32_e32 v121, v51, v115
	v_cmp_eq_f32_e64 s[76:77], v51, v115
	v_add_f32_dpp v128, v128, v128 row_ror:4 row_mask:0xf bank_mask:0xf
	v_exp_f32_e32 v165, v120
	v_max_f32_dpp v114, v114, v114 row_ror:1 row_mask:0xf bank_mask:0xf
	v_cndmask_b32_e64 v119, v119, 5, s[74:75]
	v_add_f32_dpp v128, v128, v128 row_ror:8 row_mask:0xf bank_mask:0xf
	v_sub_f32_e32 v120, v47, v115
	v_rcp_f32_e32 v244, v128
	v_cmp_eq_f32_e64 s[72:73], v47, v115
	v_pk_mul_f32 v[134:135], v[244:245], v[134:135] op_sel_hi:[0,1]
	v_exp_f32_e32 v164, v121
	v_pk_mul_f32 v[136:137], v[244:245], v[136:137] op_sel_hi:[0,1]
	v_cndmask_b32_e64 v119, v119, 4, s[76:77]
	v_mfma_f32_16x16x4_f32 v[200:203], v133, v15, v[200:203]
	v_sub_f32_e32 v121, v43, v115
	v_max_f32_dpp v114, v114, v114 row_ror:2 row_mask:0xf bank_mask:0xf
	v_cmp_eq_f32_e64 s[74:75], v43, v115
	global_store_dwordx4 v108, v[134:137], s[90:91] sc1
	v_exp_f32_e32 v163, v120
	v_pk_mul_f32 v[138:139], v[244:245], v[138:139] op_sel_hi:[0,1]
	v_cndmask_b32_e64 v119, v119, 3, s[72:73]
	v_pk_mul_f32 v[140:141], v[244:245], v[140:141] op_sel_hi:[0,1]
	v_sub_f32_e32 v120, v39, v115
	v_max_f32_dpp v114, v114, v114 row_ror:4 row_mask:0xf bank_mask:0xf
	v_cmp_eq_f32_e64 s[76:77], v39, v115
	global_store_dwordx4 v108, v[138:141], s[90:91] offset:256 sc1
	v_exp_f32_e32 v162, v121
	v_cndmask_b32_e64 v119, v119, 2, s[74:75]
	v_pk_mul_f32 v[142:143], v[244:245], v[142:143] op_sel_hi:[0,1]
	v_mfma_f32_16x16x4_f32 v[204:207], v133, v17, v[204:207]
	global_load_dwordx4 v[14:17], v104, s[86:87] offset:3072
	v_sub_f32_e32 v121, v35, v115
	v_pk_mul_f32 v[144:145], v[244:245], v[144:145] op_sel_hi:[0,1]
	v_cmp_eq_f32_e64 s[72:73], v35, v115
	global_store_dwordx4 v108, v[142:145], s[90:91] offset:512 sc1
	v_exp_f32_e32 v161, v120
	v_max_f32_dpp v114, v114, v114 row_ror:8 row_mask:0xf bank_mask:0xf
	v_cndmask_b32_e64 v119, v119, 1, s[76:77]
	v_pk_mul_f32 v[146:147], v[244:245], v[146:147] op_sel_hi:[0,1]
	v_exp_f32_e32 v160, v121
	v_pk_mul_f32 v[148:149], v[244:245], v[148:149] op_sel_hi:[0,1]
	v_cndmask_b32_e64 v119, v119, 0, s[72:73]
	global_store_dwordx4 v108, v[146:149], s[90:91] offset:768 sc1
	v_sub_f32_e32 v120, v96, v114
	v_cmp_eq_f32_e64 s[72:73], v96, v114
	s_waitcnt vmcnt(14)
	s_waitcnt vmcnt(28)
	v_mfma_f32_16x16x4_f32 v[208:211], v132, v18, 0
	v_sub_f32_e32 v121, v92, v114
	v_add_u32_e32 v113, s83, v106
	v_cmp_eq_f32_e64 s[74:75], v92, v114
	ds_read2st64_b32 v[250:251], v113 offset1:12
	v_exp_f32_e32 v149, v120
	ds_read2st64_b32 v[252:253], v113 offset0:24 offset1:36
	v_cndmask_b32_e64 v118, v155, 15, s[72:73]
	v_max3_f32 v115, v37, v41, v45
	v_sub_f32_e32 v120, v88, v114
	v_and_b32_e32 v123, 12, v119
	v_cmp_eq_f32_e64 s[76:77], v88, v114
	v_and_b32_e32 v125, 3, v119
	v_exp_f32_e32 v148, v121
	v_add_f32_e32 v129, v160, v161
	v_cndmask_b32_e64 v118, v118, 14, s[74:75]
	v_add_f32_e32 v131, v162, v163
	v_mfma_f32_16x16x4_f32 v[212:215], v132, v20, 0
	v_sub_f32_e32 v121, v84, v114
	v_max3_f32 v117, v49, v53, v57
	v_cmp_eq_f32_e64 s[72:73], v84, v114
	v_lshl_or_b32 v123, v123, 4, v125
	v_exp_f32_e32 v147, v120
	v_cndmask_b32_e64 v118, v118, 13, s[76:77]
	v_add_f32_e32 v129, v129, v164
	v_sub_f32_e32 v120, v80, v114
	v_add_f32_e32 v131, v131, v165
	v_cmp_eq_f32_e64 s[74:75], v80, v114
	v_or_b32_e32 v123, v123, v102
	v_exp_f32_e32 v146, v121
	v_max3_f32 v115, v115, v61, v65
	v_cndmask_b32_e64 v118, v118, 12, s[72:73]
	v_add_f32_e32 v129, v129, v166
	v_mfma_f32_16x16x4_f32 v[208:211], v133, v19, v[208:211]
	v_sub_f32_e32 v121, v76, v114
	v_add_f32_e32 v131, v131, v167
	v_cmp_eq_f32_e64 s[76:77], v76, v114
	v_max_u32_e32 v127, v123, v119
	v_exp_f32_e32 v145, v120
	v_max3_f32 v117, v117, v69, v73
	v_cndmask_b32_e64 v118, v118, 11, s[74:75]
	v_add_f32_e32 v129, v129, v168
	v_sub_f32_e32 v120, v72, v114
	v_add_f32_e32 v131, v131, v169
	v_cmp_eq_f32_e64 s[72:73], v72, v114
	v_min_u32_dpp v127, v127, v127 row_ror:1 row_mask:0xf bank_mask:0xf
	v_exp_f32_e32 v144, v121
	v_add_f32_e32 v129, v129, v170
	v_cndmask_b32_e64 v118, v118, 10, s[76:77]
	v_mfma_f32_16x16x4_f32 v[212:215], v133, v21, v[212:215]
	global_load_dwordx4 v[18:21], v104, s[88:89]
	v_sub_f32_e32 v121, v68, v114
	v_max3_f32 v115, v115, v77, v81
	v_cmp_eq_f32_e64 s[74:75], v68, v114
	v_add_f32_e32 v131, v131, v171
	v_exp_f32_e32 v143, v120
	v_min_u32_dpp v127, v127, v127 row_ror:2 row_mask:0xf bank_mask:0xf
	v_cndmask_b32_e64 v118, v118, 9, s[72:73]
	v_add_f32_e32 v129, v129, v172
	v_sub_f32_e32 v120, v64, v114
	v_max3_f32 v117, v117, v85, v89
	v_cmp_eq_f32_e64 s[76:77], v64, v114
	v_add_f32_e32 v131, v131, v173
	v_exp_f32_e32 v142, v121
	v_min_u32_dpp v127, v127, v127 row_ror:4 row_mask:0xf bank_mask:0xf
	v_cndmask_b32_e64 v118, v118, 8, s[74:75]
	v_add_f32_e32 v129, v129, v174
	s_waitcnt vmcnt(25)
	v_mfma_f32_16x16x4_f32 v[216:219], v132, v22, 0
	v_sub_f32_e32 v121, v60, v114
	v_add_f32_e32 v131, v131, v175
	v_cmp_eq_f32_e64 s[72:73], v60, v114
	v_max3_f32 v115, v115, v93, v97
	v_exp_f32_e32 v141, v120
	v_min_u32_dpp v127, v127, v127 row_ror:8 row_mask:0xf bank_mask:0xf
	v_cndmask_b32_e64 v118, v118, 7, s[76:77]
	v_add_f32_e32 v129, v129, v131
	v_sub_f32_e32 v120, v56, v114
	v_cmp_eq_f32_e64 s[74:75], v56, v114
	v_mad_u32_u24 v249, v127, 24, v107
	v_exp_f32_e32 v140, v121
	v_add_f32_dpp v129, v129, v129 row_ror:1 row_mask:0xf bank_mask:0xf
	v_cndmask_b32_e64 v118, v118, 6, s[72:73]
	v_max_f32_e32 v115, v115, v117
	v_mfma_f32_16x16x4_f32 v[220:223], v132, v24, 0
	v_sub_f32_e32 v121, v52, v114
	global_load_dword v241, v249, s[92:93]
	v_cmp_eq_f32_e64 s[76:77], v52, v114
	v_add_f32_dpp v129, v129, v129 row_ror:2 row_mask:0xf bank_mask:0xf
	v_exp_f32_e32 v139, v120
	s_nop 0
	v_add_f32_dpp v129, v129, v129 row_ror:4 row_mask:0xf bank_mask:0xf
	v_cndmask_b32_e64 v118, v118, 5, s[74:75]
	v_max_f32_dpp v115, v115, v115 row_ror:1 row_mask:0xf bank_mask:0xf
	v_sub_f32_e32 v120, v48, v114
	v_add_f32_dpp v129, v129, v129 row_ror:8 row_mask:0xf bank_mask:0xf
	v_cmp_eq_f32_e64 s[72:73], v48, v114
	v_rcp_f32_e32 v246, v129
	v_exp_f32_e32 v138, v121
	v_pk_mul_f32 v[160:161], v[246:247], v[160:161] op_sel_hi:[0,1]
	v_cndmask_b32_e64 v118, v118, 4, s[76:77]
	v_pk_mul_f32 v[162:163], v[246:247], v[162:163] op_sel_hi:[0,1]
	v_mfma_f32_16x16x4_f32 v[216:219], v133, v23, v[216:219]
	v_sub_f32_e32 v121, v44, v114
	v_max_f32_dpp v115, v115, v115 row_ror:2 row_mask:0xf bank_mask:0xf
	v_cmp_eq_f32_e64 s[74:75], v44, v114
	v_exp_f32_e32 v137, v120
	global_store_dwordx4 v109, v[160:163], s[90:91] sc1
	v_cndmask_b32_e64 v118, v118, 3, s[72:73]
	v_pk_mul_f32 v[164:165], v[246:247], v[164:165] op_sel_hi:[0,1]
	v_sub_f32_e32 v120, v40, v114
	v_pk_mul_f32 v[166:167], v[246:247], v[166:167] op_sel_hi:[0,1]
	v_cmp_eq_f32_e64 s[76:77], v40, v114
	v_max_f32_dpp v115, v115, v115 row_ror:4 row_mask:0xf bank_mask:0xf
	v_exp_f32_e32 v136, v121
	global_store_dwordx4 v109, v[164:167], s[90:91] offset:256 sc1
	v_cndmask_b32_e64 v118, v118, 2, s[74:75]
	v_pk_mul_f32 v[168:169], v[246:247], v[168:169] op_sel_hi:[0,1]
	v_mfma_f32_16x16x4_f32 v[220:223], v133, v25, v[220:223]
	global_load_dwordx4 v[22:25], v104, s[88:89] offset:1024
	v_sub_f32_e32 v121, v36, v114
	v_pk_mul_f32 v[170:171], v[246:247], v[170:171] op_sel_hi:[0,1]
	v_cmp_eq_f32_e64 s[72:73], v36, v114
	global_store_dwordx4 v109, v[168:171], s[90:91] offset:512 sc1
	v_exp_f32_e32 v135, v120
	v_max_f32_dpp v115, v115, v115 row_ror:8 row_mask:0xf bank_mask:0xf
	v_cndmask_b32_e64 v118, v118, 1, s[76:77]
	v_pk_mul_f32 v[172:173], v[246:247], v[172:173] op_sel_hi:[0,1]
	v_exp_f32_e32 v134, v121
	v_pk_mul_f32 v[174:175], v[246:247], v[174:175] op_sel_hi:[0,1]
	v_cndmask_b32_e64 v118, v118, 0, s[72:73]
	global_store_dwordx4 v109, v[172:175], s[90:91] offset:768 sc1
	v_sub_f32_e32 v120, v97, v115
	v_cmp_eq_f32_e64 s[72:73], v97, v115
	s_waitcnt lgkmcnt(0)
	s_waitcnt vmcnt(28)
	v_mfma_f32_16x16x4_f32 v[224:227], v132, v26, 0
	v_sub_f32_e32 v121, v93, v115
	v_add_f32_e32 v250, v159, v250
	v_cmp_eq_f32_e64 s[74:75], v93, v115
	v_add_f32_e32 v251, v158, v251
	v_exp_f32_e32 v175, v120
	v_cndmask_b32_e64 v119, v155, 15, s[72:73]
	v_add_f32_e32 v252, v157, v252
	v_sub_f32_e32 v120, v89, v115
	v_add_f32_e32 v253, v156, v253
	v_cmp_eq_f32_e64 s[76:77], v89, v115
	ds_write2st64_b32 v113, v250, v251 offset1:12
	v_exp_f32_e32 v174, v121
	ds_write2st64_b32 v113, v252, v253 offset0:24 offset1:36
	v_cndmask_b32_e64 v119, v119, 14, s[74:75]
	v_mfma_f32_16x16x4_f32 v[228:231], v132, v28, 0
	v_sub_f32_e32 v121, v85, v115
	v_and_b32_e32 v122, 12, v118
	v_cmp_eq_f32_e64 s[72:73], v85, v115
	v_and_b32_e32 v124, 3, v118
	v_exp_f32_e32 v173, v120
	v_add_f32_e32 v128, v134, v135
	v_cndmask_b32_e64 v119, v119, 13, s[76:77]
	v_sub_f32_e32 v120, v81, v115
	v_add_f32_e32 v130, v136, v137
	v_cmp_eq_f32_e64 s[74:75], v81, v115
	v_lshl_or_b32 v122, v122, 4, v124
	v_exp_f32_e32 v172, v121
	v_add_f32_e32 v128, v128, v138
	v_cndmask_b32_e64 v119, v119, 12, s[72:73]
	v_add_f32_e32 v130, v130, v139
	v_mfma_f32_16x16x4_f32 v[224:227], v133, v27, v[224:227]
	v_sub_f32_e32 v121, v77, v115
	v_cmp_eq_f32_e64 s[76:77], v77, v115
	v_or_b32_e32 v122, v122, v102
	v_exp_f32_e32 v171, v120
	v_add_f32_e32 v128, v128, v140
	v_cndmask_b32_e64 v119, v119, 11, s[74:75]
	v_add_f32_e32 v130, v130, v141
	v_sub_f32_e32 v120, v73, v115
	v_cmp_eq_f32_e64 s[72:73], v73, v115
	v_max_u32_e32 v126, v122, v118
	v_exp_f32_e32 v170, v121
	v_add_f32_e32 v128, v128, v142
	v_cndmask_b32_e64 v119, v119, 10, s[76:77]
	v_add_f32_e32 v130, v130, v143
	v_mfma_f32_16x16x4_f32 v[228:231], v133, v29, v[228:231]
	global_load_dwordx4 v[26:29], v104, s[88:89] offset:2048
	v_sub_f32_e32 v121, v69, v115
	v_min_u32_dpp v126, v126, v126 row_ror:1 row_mask:0xf bank_mask:0xf
	v_cmp_eq_f32_e64 s[74:75], v69, v115
	v_exp_f32_e32 v169, v120
	v_add_f32_e32 v128, v128, v144
	v_cndmask_b32_e64 v119, v119, 9, s[72:73]
	v_add_f32_e32 v130, v130, v145
	v_sub_f32_e32 v120, v65, v115
	v_min_u32_dpp v126, v126, v126 row_ror:2 row_mask:0xf bank_mask:0xf
	v_cmp_eq_f32_e64 s[76:77], v65, v115
	v_add_f32_e32 v128, v128, v146
	v_exp_f32_e32 v168, v121
	v_cndmask_b32_e64 v119, v119, 8, s[74:75]
	v_add_f32_e32 v130, v130, v147
	s_waitcnt vmcnt(25)
	v_mfma_f32_16x16x4_f32 v[232:235], v132, v30, 0
	v_sub_f32_e32 v121, v61, v115
	v_min_u32_dpp v126, v126, v126 row_ror:4 row_mask:0xf bank_mask:0xf
	v_cmp_eq_f32_e64 s[72:73], v61, v115
	v_add_f32_e32 v128, v128, v148
	v_exp_f32_e32 v167, v120
	v_cndmask_b32_e64 v119, v119, 7, s[76:77]
	v_add_f32_e32 v130, v130, v149
	v_sub_f32_e32 v120, v57, v115
	v_min_u32_dpp v126, v126, v126 row_ror:8 row_mask:0xf bank_mask:0xf
	v_cmp_eq_f32_e64 s[74:75], v57, v115
	v_add_f32_e32 v128, v128, v130
	v_exp_f32_e32 v166, v121
	v_mad_u32_u24 v248, v126, 24, v107
	v_cndmask_b32_e64 v119, v119, 6, s[72:73]
	v_mfma_f32_16x16x4_f32 v[236:239], v132, v32, 0
	v_sub_f32_e32 v121, v53, v115
	v_add_f32_dpp v128, v128, v128 row_ror:1 row_mask:0xf bank_mask:0xf
	v_cmp_eq_f32_e64 s[76:77], v53, v115
	global_load_dword v242, v248, s[92:93]
	v_exp_f32_e32 v165, v120
	v_add_f32_dpp v128, v128, v128 row_ror:2 row_mask:0xf bank_mask:0xf
	v_cndmask_b32_e64 v119, v119, 5, s[74:75]
	v_sub_f32_e32 v120, v49, v115
	v_add_f32_dpp v128, v128, v128 row_ror:4 row_mask:0xf bank_mask:0xf
	v_cmp_eq_f32_e64 s[72:73], v49, v115
	s_nop 0
	v_add_f32_dpp v128, v128, v128 row_ror:8 row_mask:0xf bank_mask:0xf
	v_exp_f32_e32 v164, v121
	v_rcp_f32_e32 v244, v128
	v_cndmask_b32_e64 v119, v119, 4, s[76:77]
	v_pk_mul_f32 v[134:135], v[244:245], v[134:135] op_sel_hi:[0,1]
	v_mfma_f32_16x16x4_f32 v[232:235], v133, v31, v[232:235]
	v_sub_f32_e32 v121, v45, v115
	v_cmp_eq_f32_e64 s[74:75], v45, v115
	v_pk_mul_f32 v[136:137], v[244:245], v[136:137] op_sel_hi:[0,1]
	v_exp_f32_e32 v163, v120
	global_store_dwordx4 v110, v[134:137], s[90:91] sc1
	v_cndmask_b32_e64 v119, v119, 3, s[72:73]
	v_pk_mul_f32 v[138:139], v[244:245], v[138:139] op_sel_hi:[0,1]
	v_sub_f32_e32 v120, v41, v115
	v_cmp_eq_f32_e64 s[76:77], v41, v115
	v_pk_mul_f32 v[140:141], v[244:245], v[140:141] op_sel_hi:[0,1]
	v_exp_f32_e32 v162, v121
	global_store_dwordx4 v110, v[138:141], s[90:91] offset:256 sc1
	v_cndmask_b32_e64 v119, v119, 2, s[74:75]
	v_pk_mul_f32 v[142:143], v[244:245], v[142:143] op_sel_hi:[0,1]
	v_mfma_f32_16x16x4_f32 v[236:239], v133, v33, v[236:239]
	global_load_dwordx4 v[30:33], v104, s[88:89] offset:3072
	v_sub_f32_e32 v121, v37, v115
	v_pk_mul_f32 v[144:145], v[244:245], v[144:145] op_sel_hi:[0,1]
	v_cmp_eq_f32_e64 s[72:73], v37, v115
	v_exp_f32_e32 v161, v120
	global_store_dwordx4 v110, v[142:145], s[90:91] offset:512 sc1
	v_cndmask_b32_e64 v119, v119, 1, s[76:77]
	v_pk_mul_f32 v[146:147], v[244:245], v[146:147] op_sel_hi:[0,1]
	v_exp_f32_e32 v160, v121
	v_pk_mul_f32 v[148:149], v[244:245], v[148:149] op_sel_hi:[0,1]
	v_cndmask_b32_e64 v119, v119, 0, s[72:73]
	global_store_dwordx4 v110, v[146:149], s[90:91] offset:768 sc1
	v_and_b32_e32 v123, 12, v119
	v_max3_f32 v114, v176, v180, v184
	v_and_b32_e32 v125, 3, v119
	v_add_f32_e32 v129, v160, v161
	v_add_f32_e32 v131, v162, v163
	v_max3_f32 v116, v188, v192, v196
	v_lshl_or_b32 v123, v123, 4, v125
	v_add_f32_e32 v129, v129, v164
	v_add_f32_e32 v131, v131, v165
	v_or_b32_e32 v123, v123, v102
	v_max3_f32 v114, v114, v200, v204
	v_add_f32_e32 v129, v129, v166
	v_add_f32_e32 v131, v131, v167
	v_max_u32_e32 v127, v123, v119
	v_max3_f32 v116, v116, v208, v212
	v_add_f32_e32 v129, v129, v168
	v_add_f32_e32 v131, v131, v169
	v_min_u32_dpp v127, v127, v127 row_ror:1 row_mask:0xf bank_mask:0xf
	v_add_f32_e32 v129, v129, v170
	v_max3_f32 v114, v114, v216, v220
	v_add_f32_e32 v131, v131, v171
	v_min_u32_dpp v127, v127, v127 row_ror:2 row_mask:0xf bank_mask:0xf
	v_add_f32_e32 v129, v129, v172
	v_max3_f32 v116, v116, v224, v228
	v_add_f32_e32 v131, v131, v173
	v_min_u32_dpp v127, v127, v127 row_ror:4 row_mask:0xf bank_mask:0xf
	v_add_f32_e32 v129, v129, v174
	v_add_f32_e32 v131, v131, v175
	v_max3_f32 v114, v114, v232, v236
	v_min_u32_dpp v127, v127, v127 row_ror:8 row_mask:0xf bank_mask:0xf
	v_add_f32_e32 v129, v129, v131
	v_mad_u32_u24 v249, v127, 24, v107
	s_nop 0
	v_add_f32_dpp v129, v129, v129 row_ror:1 row_mask:0xf bank_mask:0xf
	v_max_f32_e32 v114, v114, v116
	global_load_dword v243, v249, s[92:93]
	v_add_f32_dpp v129, v129, v129 row_ror:2 row_mask:0xf bank_mask:0xf
	s_nop 1
	v_add_f32_dpp v129, v129, v129 row_ror:4 row_mask:0xf bank_mask:0xf
	v_max_f32_dpp v114, v114, v114 row_ror:1 row_mask:0xf bank_mask:0xf
	s_nop 0
	v_add_f32_dpp v129, v129, v129 row_ror:8 row_mask:0xf bank_mask:0xf
	v_rcp_f32_e32 v246, v129
	s_nop 0
	v_pk_mul_f32 v[160:161], v[246:247], v[160:161] op_sel_hi:[0,1]
	v_pk_mul_f32 v[162:163], v[246:247], v[162:163] op_sel_hi:[0,1]
	v_max_f32_dpp v114, v114, v114 row_ror:2 row_mask:0xf bank_mask:0xf
	global_store_dwordx4 v111, v[160:163], s[90:91] sc1
	v_pk_mul_f32 v[164:165], v[246:247], v[164:165] op_sel_hi:[0,1]
	v_pk_mul_f32 v[166:167], v[246:247], v[166:167] op_sel_hi:[0,1]
	v_max_f32_dpp v114, v114, v114 row_ror:4 row_mask:0xf bank_mask:0xf
	global_store_dwordx4 v111, v[164:167], s[90:91] offset:256 sc1
	v_pk_mul_f32 v[168:169], v[246:247], v[168:169] op_sel_hi:[0,1]
	v_pk_mul_f32 v[170:171], v[246:247], v[170:171] op_sel_hi:[0,1]
	global_store_dwordx4 v111, v[168:171], s[90:91] offset:512 sc1
	v_max_f32_dpp v114, v114, v114 row_ror:8 row_mask:0xf bank_mask:0xf
	v_pk_mul_f32 v[172:173], v[246:247], v[172:173] op_sel_hi:[0,1]
	v_pk_mul_f32 v[174:175], v[246:247], v[174:175] op_sel_hi:[0,1]
	global_store_dwordx4 v111, v[172:175], s[90:91] offset:768 sc1
	s_add_i32 s70, s70, 1
	s_waitcnt lgkmcnt(0)
	s_lshl_b32 s84, s70, 13
	s_add_u32 s90, s80, s84
	s_addc_u32 s91, s81, 0
	s_mul_i32 s84, s70, 0xc000
	s_add_u32 s92, s94, s84
	s_addc_u32 s93, s95, 0
	s_add_i32 s84, s70, 2
	s_and_b32 s84, s84, 15
	s_lshl_b32 s82, s84, 12
	s_lshl_b32 s84, s84, 16
	s_add_u32 s84, s84, 0x787000
	s_add_u32 s86, s40, s84
	s_addc_u32 s87, s41, 0
	s_add_u32 s88, s86, 0x1000
	s_addc_u32 s89, s87, 0
	s_add_i32 s84, s70, 15
	s_and_b32 s84, s84, 15
	s_mul_i32 s84, s84, 0xc0
	s_add_u32 s83, s84, 0x10000
	v_add_u32_e32 v112, s82, v105
	s_add_i32 s84, s70, 4
	s_and_b32 s84, s84, 15
	s_lshl_b32 s84, s84, 16
	s_add_u32 s84, s84, 0x787000
	s_add_u32 s58, s40, s84
	s_addc_u32 s59, s41, 0
	global_load_dword v98, v100, s[58:59]
	v_sub_f32_e32 v120, v236, v114
	v_cmp_eq_f32_e64 s[72:73], v236, v114
	s_waitcnt vmcnt(28)
	v_mfma_f32_16x16x4_f32 v[34:37], v254, v6, 0
	ds_read2st64_b32 v[132:133], v112 offset1:1
	v_sub_f32_e32 v121, v232, v114
	v_cmp_eq_f32_e64 s[74:75], v232, v114
	v_exp_f32_e32 v149, v120
	v_cndmask_b32_e64 v118, v155, 15, s[72:73]
	v_max3_f32 v115, v177, v181, v185
	v_sub_f32_e32 v120, v228, v114
	v_cmp_eq_f32_e64 s[76:77], v228, v114
	v_exp_f32_e32 v148, v121
	v_cndmask_b32_e64 v118, v118, 14, s[74:75]
	v_mfma_f32_16x16x4_f32 v[38:41], v254, v8, 0
	v_sub_f32_e32 v121, v224, v114
	v_max3_f32 v117, v189, v193, v197
	v_cmp_eq_f32_e64 s[72:73], v224, v114
	v_exp_f32_e32 v147, v120
	v_cndmask_b32_e64 v118, v118, 13, s[76:77]
	v_sub_f32_e32 v120, v220, v114
	v_cmp_eq_f32_e64 s[74:75], v220, v114
	v_max3_f32 v115, v115, v201, v205
	v_exp_f32_e32 v146, v121
	v_cndmask_b32_e64 v118, v118, 12, s[72:73]
	v_mfma_f32_16x16x4_f32 v[34:37], v255, v7, v[34:37]
	v_sub_f32_e32 v121, v216, v114
	v_cmp_eq_f32_e64 s[76:77], v216, v114
	v_exp_f32_e32 v145, v120
	v_cndmask_b32_e64 v118, v118, 11, s[74:75]
	v_max3_f32 v117, v117, v209, v213
	v_sub_f32_e32 v120, v212, v114
	v_cmp_eq_f32_e64 s[72:73], v212, v114
	v_exp_f32_e32 v144, v121
	v_cndmask_b32_e64 v118, v118, 10, s[76:77]
	v_mfma_f32_16x16x4_f32 v[38:41], v255, v9, v[38:41]
	global_load_dwordx4 v[6:9], v104, s[86:87]
	v_sub_f32_e32 v121, v208, v114
	v_max3_f32 v115, v115, v217, v221
	v_cmp_eq_f32_e64 s[74:75], v208, v114
	v_exp_f32_e32 v143, v120
	v_cndmask_b32_e64 v118, v118, 9, s[72:73]
	v_sub_f32_e32 v120, v204, v114
	v_cmp_eq_f32_e64 s[76:77], v204, v114
	v_max3_f32 v117, v117, v225, v229
	v_exp_f32_e32 v142, v121
	v_cndmask_b32_e64 v118, v118, 8, s[74:75]
	s_waitcnt vmcnt(28)
	v_mfma_f32_16x16x4_f32 v[42:45], v254, v2, 0
	v_sub_f32_e32 v121, v200, v114
	v_cmp_eq_f32_e64 s[72:73], v200, v114
	v_exp_f32_e32 v141, v120
	v_cndmask_b32_e64 v118, v118, 7, s[76:77]
	v_max3_f32 v115, v115, v233, v237
	v_sub_f32_e32 v120, v196, v114
	v_cmp_eq_f32_e64 s[74:75], v196, v114
	v_exp_f32_e32 v140, v121
	v_cndmask_b32_e64 v118, v118, 6, s[72:73]
	v_mfma_f32_16x16x4_f32 v[46:49], v254, v4, 0
	v_sub_f32_e32 v121, v192, v114
	v_max_f32_e32 v115, v115, v117
	v_cmp_eq_f32_e64 s[76:77], v192, v114
	v_exp_f32_e32 v139, v120
	v_cndmask_b32_e64 v118, v118, 5, s[74:75]
	v_sub_f32_e32 v120, v188, v114
	v_cmp_eq_f32_e64 s[72:73], v188, v114
	v_max_f32_dpp v115, v115, v115 row_ror:1 row_mask:0xf bank_mask:0xf
	v_exp_f32_e32 v138, v121
	v_cndmask_b32_e64 v118, v118, 4, s[76:77]
	v_mfma_f32_16x16x4_f32 v[42:45], v255, v3, v[42:45]
	v_sub_f32_e32 v121, v184, v114
	v_cmp_eq_f32_e64 s[74:75], v184, v114
	v_exp_f32_e32 v137, v120
	v_cndmask_b32_e64 v118, v118, 3, s[72:73]
	v_max_f32_dpp v115, v115, v115 row_ror:2 row_mask:0xf bank_mask:0xf
	v_sub_f32_e32 v120, v180, v114
	v_cmp_eq_f32_e64 s[76:77], v180, v114
	v_exp_f32_e32 v136, v121
	v_cndmask_b32_e64 v118, v118, 2, s[74:75]
	v_mfma_f32_16x16x4_f32 v[46:49], v255, v5, v[46:49]
	global_load_dwordx4 v[2:5], v104, s[86:87] offset:1024
	v_sub_f32_e32 v121, v176, v114
	v_max_f32_dpp v115, v115, v115 row_ror:4 row_mask:0xf bank_mask:0xf
	v_cmp_eq_f32_e64 s[72:73], v176, v114
	v_exp_f32_e32 v135, v120
	v_cndmask_b32_e64 v118, v118, 1, s[76:77]
	v_exp_f32_e32 v134, v121
	v_cndmask_b32_e64 v118, v118, 0, s[72:73]
	v_max_f32_dpp v115, v115, v115 row_ror:8 row_mask:0xf bank_mask:0xf
	v_sub_f32_e32 v120, v237, v115
	v_cmp_eq_f32_e64 s[72:73], v237, v115
	v_max3_f32 v114, v178, v182, v186
	s_waitcnt vmcnt(28)
	v_mfma_f32_16x16x4_f32 v[50:53], v254, v10, 0
	v_sub_f32_e32 v121, v233, v115
	v_and_b32_e32 v122, 12, v118
	v_cmp_eq_f32_e64 s[74:75], v233, v115
	v_and_b32_e32 v124, 3, v118
	v_exp_f32_e32 v175, v120
	v_add_f32_e32 v128, v134, v135
	v_cndmask_b32_e64 v119, v155, 15, s[72:73]
	v_add_f32_e32 v130, v136, v137
	v_sub_f32_e32 v120, v229, v115
	v_max3_f32 v116, v190, v194, v198
	v_cmp_eq_f32_e64 s[76:77], v229, v115
	v_exp_f32_e32 v174, v121
	v_lshl_or_b32 v122, v122, 4, v124
	v_cndmask_b32_e64 v119, v119, 14, s[74:75]
	v_add_f32_e32 v128, v128, v138
	v_mfma_f32_16x16x4_f32 v[54:57], v254, v12, 0
	v_sub_f32_e32 v121, v225, v115
	v_add_f32_e32 v130, v130, v139
	v_cmp_eq_f32_e64 s[72:73], v225, v115
	v_or_b32_e32 v122, v122, v102
	v_exp_f32_e32 v173, v120
	v_max3_f32 v114, v114, v202, v206
	v_cndmask_b32_e64 v119, v119, 13, s[76:77]
	v_add_f32_e32 v128, v128, v140
	v_sub_f32_e32 v120, v221, v115
	v_cmp_eq_f32_e64 s[74:75], v221, v115
	v_add_f32_e32 v130, v130, v141
	v_exp_f32_e32 v172, v121
	v_max_u32_e32 v126, v122, v118
	v_cndmask_b32_e64 v119, v119, 12, s[72:73]
	v_max3_f32 v116, v116, v210, v214
	v_mfma_f32_16x16x4_f32 v[50:53], v255, v11, v[50:53]
	v_sub_f32_e32 v121, v217, v115
	v_add_f32_e32 v128, v128, v142
	v_cmp_eq_f32_e64 s[76:77], v217, v115
	v_add_f32_e32 v130, v130, v143
	v_exp_f32_e32 v171, v120
	v_min_u32_dpp v126, v126, v126 row_ror:1 row_mask:0xf bank_mask:0xf
	v_cndmask_b32_e64 v119, v119, 11, s[74:75]
	v_sub_f32_e32 v120, v213, v115
	v_add_f32_e32 v128, v128, v144
	v_cmp_eq_f32_e64 s[72:73], v213, v115
	v_max3_f32 v114, v114, v218, v222
	v_exp_f32_e32 v170, v121
	v_add_f32_e32 v130, v130, v145
	v_cndmask_b32_e64 v119, v119, 10, s[76:77]
	v_min_u32_dpp v126, v126, v126 row_ror:2 row_mask:0xf bank_mask:0xf
	v_mfma_f32_16x16x4_f32 v[54:57], v255, v13, v[54:57]
	global_load_dwordx4 v[10:13], v104, s[86:87] offset:2048
	v_sub_f32_e32 v121, v209, v115
	v_add_f32_e32 v128, v128, v146
	v_cmp_eq_f32_e64 s[74:75], v209, v115
	v_max3_f32 v116, v116, v226, v230
	v_exp_f32_e32 v169, v120
	v_cndmask_b32_e64 v119, v119, 9, s[72:73]
	v_add_f32_e32 v130, v130, v147
	v_sub_f32_e32 v120, v205, v115
	v_min_u32_dpp v126, v126, v126 row_ror:4 row_mask:0xf bank_mask:0xf
	v_cmp_eq_f32_e64 s[76:77], v205, v115
	v_add_f32_e32 v128, v128, v148
	v_exp_f32_e32 v168, v121
	v_add_f32_e32 v130, v130, v149
	v_cndmask_b32_e64 v119, v119, 8, s[74:75]
	v_max3_f32 v114, v114, v234, v238
	s_waitcnt vmcnt(25)
	v_mfma_f32_16x16x4_f32 v[58:61], v254, v14, 0
	v_sub_f32_e32 v121, v201, v115
	v_min_u32_dpp v126, v126, v126 row_ror:8 row_mask:0xf bank_mask:0xf
	v_cmp_eq_f32_e64 s[72:73], v201, v115
	v_exp_f32_e32 v167, v120
	v_add_f32_e32 v128, v128, v130
	v_cndmask_b32_e64 v119, v119, 7, s[76:77]
	v_mad_u32_u24 v248, v126, 24, v107
	v_sub_f32_e32 v120, v197, v115
	v_add_f32_dpp v128, v128, v128 row_ror:1 row_mask:0xf bank_mask:0xf
	v_cmp_eq_f32_e64 s[74:75], v197, v115
	v_max_f32_e32 v114, v114, v116
	v_exp_f32_e32 v166, v121
	global_load_dword v159, v248, s[92:93]
	v_cndmask_b32_e64 v119, v119, 6, s[72:73]
	v_add_f32_dpp v128, v128, v128 row_ror:2 row_mask:0xf bank_mask:0xf
	v_mfma_f32_16x16x4_f32 v[62:65], v254, v16, 0
	v_sub_f32_e32 v121, v193, v115
	v_cmp_eq_f32_e64 s[76:77], v193, v115
	v_add_f32_dpp v128, v128, v128 row_ror:4 row_mask:0xf bank_mask:0xf
	v_exp_f32_e32 v165, v120
	v_max_f32_dpp v114, v114, v114 row_ror:1 row_mask:0xf bank_mask:0xf
	v_cndmask_b32_e64 v119, v119, 5, s[74:75]
	v_add_f32_dpp v128, v128, v128 row_ror:8 row_mask:0xf bank_mask:0xf
	v_sub_f32_e32 v120, v189, v115
	v_rcp_f32_e32 v244, v128
	v_cmp_eq_f32_e64 s[72:73], v189, v115
	v_pk_mul_f32 v[134:135], v[244:245], v[134:135] op_sel_hi:[0,1]
	v_exp_f32_e32 v164, v121
	v_pk_mul_f32 v[136:137], v[244:245], v[136:137] op_sel_hi:[0,1]
	v_cndmask_b32_e64 v119, v119, 4, s[76:77]
	v_mfma_f32_16x16x4_f32 v[58:61], v255, v15, v[58:61]
	v_sub_f32_e32 v121, v185, v115
	v_max_f32_dpp v114, v114, v114 row_ror:2 row_mask:0xf bank_mask:0xf
	v_cmp_eq_f32_e64 s[74:75], v185, v115
	global_store_dwordx4 v108, v[134:137], s[90:91] sc1
	v_exp_f32_e32 v163, v120
	v_pk_mul_f32 v[138:139], v[244:245], v[138:139] op_sel_hi:[0,1]
	v_cndmask_b32_e64 v119, v119, 3, s[72:73]
	v_pk_mul_f32 v[140:141], v[244:245], v[140:141] op_sel_hi:[0,1]
	v_sub_f32_e32 v120, v181, v115
	v_max_f32_dpp v114, v114, v114 row_ror:4 row_mask:0xf bank_mask:0xf
	v_cmp_eq_f32_e64 s[76:77], v181, v115
	global_store_dwordx4 v108, v[138:141], s[90:91] offset:256 sc1
	v_exp_f32_e32 v162, v121
	v_cndmask_b32_e64 v119, v119, 2, s[74:75]
	v_pk_mul_f32 v[142:143], v[244:245], v[142:143] op_sel_hi:[0,1]
	v_mfma_f32_16x16x4_f32 v[62:65], v255, v17, v[62:65]
	global_load_dwordx4 v[14:17], v104, s[86:87] offset:3072
	v_sub_f32_e32 v121, v177, v115
	v_pk_mul_f32 v[144:145], v[244:245], v[144:145] op_sel_hi:[0,1]
	v_cmp_eq_f32_e64 s[72:73], v177, v115
	global_store_dwordx4 v108, v[142:145], s[90:91] offset:512 sc1
	v_exp_f32_e32 v161, v120
	v_max_f32_dpp v114, v114, v114 row_ror:8 row_mask:0xf bank_mask:0xf
	v_cndmask_b32_e64 v119, v119, 1, s[76:77]
	v_pk_mul_f32 v[146:147], v[244:245], v[146:147] op_sel_hi:[0,1]
	v_exp_f32_e32 v160, v121
	v_pk_mul_f32 v[148:149], v[244:245], v[148:149] op_sel_hi:[0,1]
	v_cndmask_b32_e64 v119, v119, 0, s[72:73]
	global_store_dwordx4 v108, v[146:149], s[90:91] offset:768 sc1
	v_sub_f32_e32 v120, v238, v114
	v_cmp_eq_f32_e64 s[72:73], v238, v114
	s_waitcnt vmcnt(14)
	s_waitcnt vmcnt(28)
	v_mfma_f32_16x16x4_f32 v[66:69], v254, v18, 0
	v_sub_f32_e32 v121, v234, v114
	v_add_u32_e32 v113, s83, v106
	v_cmp_eq_f32_e64 s[74:75], v234, v114
	ds_read2st64_b32 v[250:251], v113 offset1:12
	v_exp_f32_e32 v149, v120
	ds_read2st64_b32 v[252:253], v113 offset0:24 offset1:36
	v_cndmask_b32_e64 v118, v155, 15, s[72:73]
	v_max3_f32 v115, v179, v183, v187
	v_sub_f32_e32 v120, v230, v114
	v_and_b32_e32 v123, 12, v119
	v_cmp_eq_f32_e64 s[76:77], v230, v114
	v_and_b32_e32 v125, 3, v119
	v_exp_f32_e32 v148, v121
	v_add_f32_e32 v129, v160, v161
	v_cndmask_b32_e64 v118, v118, 14, s[74:75]
	v_add_f32_e32 v131, v162, v163
	v_mfma_f32_16x16x4_f32 v[70:73], v254, v20, 0
	v_sub_f32_e32 v121, v226, v114
	v_max3_f32 v117, v191, v195, v199
	v_cmp_eq_f32_e64 s[72:73], v226, v114
	v_lshl_or_b32 v123, v123, 4, v125
	v_exp_f32_e32 v147, v120
	v_cndmask_b32_e64 v118, v118, 13, s[76:77]
	v_add_f32_e32 v129, v129, v164
	v_sub_f32_e32 v120, v222, v114
	v_add_f32_e32 v131, v131, v165
	v_cmp_eq_f32_e64 s[74:75], v222, v114
	v_or_b32_e32 v123, v123, v102
	v_exp_f32_e32 v146, v121
	v_max3_f32 v115, v115, v203, v207
	v_cndmask_b32_e64 v118, v118, 12, s[72:73]
	v_add_f32_e32 v129, v129, v166
	v_mfma_f32_16x16x4_f32 v[66:69], v255, v19, v[66:69]
	v_sub_f32_e32 v121, v218, v114
	v_add_f32_e32 v131, v131, v167
	v_cmp_eq_f32_e64 s[76:77], v218, v114
	v_max_u32_e32 v127, v123, v119
	v_exp_f32_e32 v145, v120
	v_max3_f32 v117, v117, v211, v215
	v_cndmask_b32_e64 v118, v118, 11, s[74:75]
	v_add_f32_e32 v129, v129, v168
	v_sub_f32_e32 v120, v214, v114
	v_add_f32_e32 v131, v131, v169
	v_cmp_eq_f32_e64 s[72:73], v214, v114
	v_min_u32_dpp v127, v127, v127 row_ror:1 row_mask:0xf bank_mask:0xf
	v_exp_f32_e32 v144, v121
	v_add_f32_e32 v129, v129, v170
	v_cndmask_b32_e64 v118, v118, 10, s[76:77]
	v_mfma_f32_16x16x4_f32 v[70:73], v255, v21, v[70:73]
	global_load_dwordx4 v[18:21], v104, s[88:89]
	v_sub_f32_e32 v121, v210, v114
	v_max3_f32 v115, v115, v219, v223
	v_cmp_eq_f32_e64 s[74:75], v210, v114
	v_add_f32_e32 v131, v131, v171
	v_exp_f32_e32 v143, v120
	v_min_u32_dpp v127, v127, v127 row_ror:2 row_mask:0xf bank_mask:0xf
	v_cndmask_b32_e64 v118, v118, 9, s[72:73]
	v_add_f32_e32 v129, v129, v172
	v_sub_f32_e32 v120, v206, v114
	v_max3_f32 v117, v117, v227, v231
	v_cmp_eq_f32_e64 s[76:77], v206, v114
	v_add_f32_e32 v131, v131, v173
	v_exp_f32_e32 v142, v121
	v_min_u32_dpp v127, v127, v127 row_ror:4 row_mask:0xf bank_mask:0xf
	v_cndmask_b32_e64 v118, v118, 8, s[74:75]
	v_add_f32_e32 v129, v129, v174
	s_waitcnt vmcnt(25)
	v_mfma_f32_16x16x4_f32 v[74:77], v254, v22, 0
	v_sub_f32_e32 v121, v202, v114
	v_add_f32_e32 v131, v131, v175
	v_cmp_eq_f32_e64 s[72:73], v202, v114
	v_max3_f32 v115, v115, v235, v239
	v_exp_f32_e32 v141, v120
	v_min_u32_dpp v127, v127, v127 row_ror:8 row_mask:0xf bank_mask:0xf
	v_cndmask_b32_e64 v118, v118, 7, s[76:77]
	v_add_f32_e32 v129, v129, v131
	v_sub_f32_e32 v120, v198, v114
	v_cmp_eq_f32_e64 s[74:75], v198, v114
	v_mad_u32_u24 v249, v127, 24, v107
	v_exp_f32_e32 v140, v121
	v_add_f32_dpp v129, v129, v129 row_ror:1 row_mask:0xf bank_mask:0xf
	v_cndmask_b32_e64 v118, v118, 6, s[72:73]
	v_max_f32_e32 v115, v115, v117
	v_mfma_f32_16x16x4_f32 v[78:81], v254, v24, 0
	v_sub_f32_e32 v121, v194, v114
	global_load_dword v158, v249, s[92:93]
	v_cmp_eq_f32_e64 s[76:77], v194, v114
	v_add_f32_dpp v129, v129, v129 row_ror:2 row_mask:0xf bank_mask:0xf
	v_exp_f32_e32 v139, v120
	s_nop 0
	v_add_f32_dpp v129, v129, v129 row_ror:4 row_mask:0xf bank_mask:0xf
	v_cndmask_b32_e64 v118, v118, 5, s[74:75]
	v_max_f32_dpp v115, v115, v115 row_ror:1 row_mask:0xf bank_mask:0xf
	v_sub_f32_e32 v120, v190, v114
	v_add_f32_dpp v129, v129, v129 row_ror:8 row_mask:0xf bank_mask:0xf
	v_cmp_eq_f32_e64 s[72:73], v190, v114
	v_rcp_f32_e32 v246, v129
	v_exp_f32_e32 v138, v121
	v_pk_mul_f32 v[160:161], v[246:247], v[160:161] op_sel_hi:[0,1]
	v_cndmask_b32_e64 v118, v118, 4, s[76:77]
	v_pk_mul_f32 v[162:163], v[246:247], v[162:163] op_sel_hi:[0,1]
	v_mfma_f32_16x16x4_f32 v[74:77], v255, v23, v[74:77]
	v_sub_f32_e32 v121, v186, v114
	v_max_f32_dpp v115, v115, v115 row_ror:2 row_mask:0xf bank_mask:0xf
	v_cmp_eq_f32_e64 s[74:75], v186, v114
	v_exp_f32_e32 v137, v120
	global_store_dwordx4 v109, v[160:163], s[90:91] sc1
	v_cndmask_b32_e64 v118, v118, 3, s[72:73]
	v_pk_mul_f32 v[164:165], v[246:247], v[164:165] op_sel_hi:[0,1]
	v_sub_f32_e32 v120, v182, v114
	v_pk_mul_f32 v[166:167], v[246:247], v[166:167] op_sel_hi:[0,1]
	v_cmp_eq_f32_e64 s[76:77], v182, v114
	v_max_f32_dpp v115, v115, v115 row_ror:4 row_mask:0xf bank_mask:0xf
	v_exp_f32_e32 v136, v121
	global_store_dwordx4 v109, v[164:167], s[90:91] offset:256 sc1
	v_cndmask_b32_e64 v118, v118, 2, s[74:75]
	v_pk_mul_f32 v[168:169], v[246:247], v[168:169] op_sel_hi:[0,1]
	v_mfma_f32_16x16x4_f32 v[78:81], v255, v25, v[78:81]
	global_load_dwordx4 v[22:25], v104, s[88:89] offset:1024
	v_sub_f32_e32 v121, v178, v114
	v_pk_mul_f32 v[170:171], v[246:247], v[170:171] op_sel_hi:[0,1]
	v_cmp_eq_f32_e64 s[72:73], v178, v114
	global_store_dwordx4 v109, v[168:171], s[90:91] offset:512 sc1
	v_exp_f32_e32 v135, v120
	v_max_f32_dpp v115, v115, v115 row_ror:8 row_mask:0xf bank_mask:0xf
	v_cndmask_b32_e64 v118, v118, 1, s[76:77]
	v_pk_mul_f32 v[172:173], v[246:247], v[172:173] op_sel_hi:[0,1]
	v_exp_f32_e32 v134, v121
	v_pk_mul_f32 v[174:175], v[246:247], v[174:175] op_sel_hi:[0,1]
	v_cndmask_b32_e64 v118, v118, 0, s[72:73]
	global_store_dwordx4 v109, v[172:175], s[90:91] offset:768 sc1
	v_sub_f32_e32 v120, v239, v115
	v_cmp_eq_f32_e64 s[72:73], v239, v115
	s_waitcnt lgkmcnt(0)
	s_waitcnt vmcnt(28)
	v_mfma_f32_16x16x4_f32 v[82:85], v254, v26, 0
	v_sub_f32_e32 v121, v235, v115
	v_add_f32_e32 v250, v240, v250
	v_cmp_eq_f32_e64 s[74:75], v235, v115
	v_add_f32_e32 v251, v241, v251
	v_exp_f32_e32 v175, v120
	v_cndmask_b32_e64 v119, v155, 15, s[72:73]
	v_add_f32_e32 v252, v242, v252
	v_sub_f32_e32 v120, v231, v115
	v_add_f32_e32 v253, v243, v253
	v_cmp_eq_f32_e64 s[76:77], v231, v115
	ds_write2st64_b32 v113, v250, v251 offset1:12
	v_exp_f32_e32 v174, v121
	ds_write2st64_b32 v113, v252, v253 offset0:24 offset1:36
	v_cndmask_b32_e64 v119, v119, 14, s[74:75]
	v_mfma_f32_16x16x4_f32 v[86:89], v254, v28, 0
	v_sub_f32_e32 v121, v227, v115
	v_and_b32_e32 v122, 12, v118
	v_cmp_eq_f32_e64 s[72:73], v227, v115
	v_and_b32_e32 v124, 3, v118
	v_exp_f32_e32 v173, v120
	v_add_f32_e32 v128, v134, v135
	v_cndmask_b32_e64 v119, v119, 13, s[76:77]
	v_sub_f32_e32 v120, v223, v115
	v_add_f32_e32 v130, v136, v137
	v_cmp_eq_f32_e64 s[74:75], v223, v115
	v_lshl_or_b32 v122, v122, 4, v124
	v_exp_f32_e32 v172, v121
	v_add_f32_e32 v128, v128, v138
	v_cndmask_b32_e64 v119, v119, 12, s[72:73]
	v_add_f32_e32 v130, v130, v139
	v_mfma_f32_16x16x4_f32 v[82:85], v255, v27, v[82:85]
	v_sub_f32_e32 v121, v219, v115
	v_cmp_eq_f32_e64 s[76:77], v219, v115
	v_or_b32_e32 v122, v122, v102
	v_exp_f32_e32 v171, v120
	v_add_f32_e32 v128, v128, v140
	v_cndmask_b32_e64 v119, v119, 11, s[74:75]
	v_add_f32_e32 v130, v130, v141
	v_sub_f32_e32 v120, v215, v115
	v_cmp_eq_f32_e64 s[72:73], v215, v115
	v_max_u32_e32 v126, v122, v118
	v_exp_f32_e32 v170, v121
	v_add_f32_e32 v128, v128, v142
	v_cndmask_b32_e64 v119, v119, 10, s[76:77]
	v_add_f32_e32 v130, v130, v143
	v_mfma_f32_16x16x4_f32 v[86:89], v255, v29, v[86:89]
	global_load_dwordx4 v[26:29], v104, s[88:89] offset:2048
	v_sub_f32_e32 v121, v211, v115
	v_min_u32_dpp v126, v126, v126 row_ror:1 row_mask:0xf bank_mask:0xf
	v_cmp_eq_f32_e64 s[74:75], v211, v115
	v_exp_f32_e32 v169, v120
	v_add_f32_e32 v128, v128, v144
	v_cndmask_b32_e64 v119, v119, 9, s[72:73]
	v_add_f32_e32 v130, v130, v145
	v_sub_f32_e32 v120, v207, v115
	v_min_u32_dpp v126, v126, v126 row_ror:2 row_mask:0xf bank_mask:0xf
	v_cmp_eq_f32_e64 s[76:77], v207, v115
	v_add_f32_e32 v128, v128, v146
	v_exp_f32_e32 v168, v121
	v_cndmask_b32_e64 v119, v119, 8, s[74:75]
	v_add_f32_e32 v130, v130, v147
	s_waitcnt vmcnt(25)
	v_mfma_f32_16x16x4_f32 v[90:93], v254, v30, 0
	v_sub_f32_e32 v121, v203, v115
	v_min_u32_dpp v126, v126, v126 row_ror:4 row_mask:0xf bank_mask:0xf
	v_cmp_eq_f32_e64 s[72:73], v203, v115
	v_add_f32_e32 v128, v128, v148
	v_exp_f32_e32 v167, v120
	v_cndmask_b32_e64 v119, v119, 7, s[76:77]
	v_add_f32_e32 v130, v130, v149
	v_sub_f32_e32 v120, v199, v115
	v_min_u32_dpp v126, v126, v126 row_ror:8 row_mask:0xf bank_mask:0xf
	v_cmp_eq_f32_e64 s[74:75], v199, v115
	v_add_f32_e32 v128, v128, v130
	v_exp_f32_e32 v166, v121
	v_mad_u32_u24 v248, v126, 24, v107
	v_cndmask_b32_e64 v119, v119, 6, s[72:73]
	v_mfma_f32_16x16x4_f32 v[94:97], v254, v32, 0
	v_sub_f32_e32 v121, v195, v115
	v_add_f32_dpp v128, v128, v128 row_ror:1 row_mask:0xf bank_mask:0xf
	v_cmp_eq_f32_e64 s[76:77], v195, v115
	global_load_dword v157, v248, s[92:93]
	v_exp_f32_e32 v165, v120
	v_add_f32_dpp v128, v128, v128 row_ror:2 row_mask:0xf bank_mask:0xf
	v_cndmask_b32_e64 v119, v119, 5, s[74:75]
	v_sub_f32_e32 v120, v191, v115
	v_add_f32_dpp v128, v128, v128 row_ror:4 row_mask:0xf bank_mask:0xf
	v_cmp_eq_f32_e64 s[72:73], v191, v115
	s_nop 0
	v_add_f32_dpp v128, v128, v128 row_ror:8 row_mask:0xf bank_mask:0xf
	v_exp_f32_e32 v164, v121
	v_rcp_f32_e32 v244, v128
	v_cndmask_b32_e64 v119, v119, 4, s[76:77]
	v_pk_mul_f32 v[134:135], v[244:245], v[134:135] op_sel_hi:[0,1]
	v_mfma_f32_16x16x4_f32 v[90:93], v255, v31, v[90:93]
	v_sub_f32_e32 v121, v187, v115
	v_cmp_eq_f32_e64 s[74:75], v187, v115
	v_pk_mul_f32 v[136:137], v[244:245], v[136:137] op_sel_hi:[0,1]
	v_exp_f32_e32 v163, v120
	global_store_dwordx4 v110, v[134:137], s[90:91] sc1
	v_cndmask_b32_e64 v119, v119, 3, s[72:73]
	v_pk_mul_f32 v[138:139], v[244:245], v[138:139] op_sel_hi:[0,1]
	v_sub_f32_e32 v120, v183, v115
	v_cmp_eq_f32_e64 s[76:77], v183, v115
	v_pk_mul_f32 v[140:141], v[244:245], v[140:141] op_sel_hi:[0,1]
	v_exp_f32_e32 v162, v121
	global_store_dwordx4 v110, v[138:141], s[90:91] offset:256 sc1
	v_cndmask_b32_e64 v119, v119, 2, s[74:75]
	v_pk_mul_f32 v[142:143], v[244:245], v[142:143] op_sel_hi:[0,1]
	v_mfma_f32_16x16x4_f32 v[94:97], v255, v33, v[94:97]
	global_load_dwordx4 v[30:33], v104, s[88:89] offset:3072
	v_sub_f32_e32 v121, v179, v115
	v_pk_mul_f32 v[144:145], v[244:245], v[144:145] op_sel_hi:[0,1]
	v_cmp_eq_f32_e64 s[72:73], v179, v115
	v_exp_f32_e32 v161, v120
	global_store_dwordx4 v110, v[142:145], s[90:91] offset:512 sc1
	v_cndmask_b32_e64 v119, v119, 1, s[76:77]
	v_pk_mul_f32 v[146:147], v[244:245], v[146:147] op_sel_hi:[0,1]
	v_exp_f32_e32 v160, v121
	v_pk_mul_f32 v[148:149], v[244:245], v[148:149] op_sel_hi:[0,1]
	v_cndmask_b32_e64 v119, v119, 0, s[72:73]
	global_store_dwordx4 v110, v[146:149], s[90:91] offset:768 sc1
	v_and_b32_e32 v123, 12, v119
	v_max3_f32 v114, v34, v38, v42
	v_and_b32_e32 v125, 3, v119
	v_add_f32_e32 v129, v160, v161
	v_add_f32_e32 v131, v162, v163
	v_max3_f32 v116, v46, v50, v54
	v_lshl_or_b32 v123, v123, 4, v125
	v_add_f32_e32 v129, v129, v164
	v_add_f32_e32 v131, v131, v165
	v_or_b32_e32 v123, v123, v102
	v_max3_f32 v114, v114, v58, v62
	v_add_f32_e32 v129, v129, v166
	v_add_f32_e32 v131, v131, v167
	v_max_u32_e32 v127, v123, v119
	v_max3_f32 v116, v116, v66, v70
	v_add_f32_e32 v129, v129, v168
	v_add_f32_e32 v131, v131, v169
	v_min_u32_dpp v127, v127, v127 row_ror:1 row_mask:0xf bank_mask:0xf
	v_add_f32_e32 v129, v129, v170
	v_max3_f32 v114, v114, v74, v78
	v_add_f32_e32 v131, v131, v171
	v_min_u32_dpp v127, v127, v127 row_ror:2 row_mask:0xf bank_mask:0xf
	v_add_f32_e32 v129, v129, v172
	v_max3_f32 v116, v116, v82, v86
	v_add_f32_e32 v131, v131, v173
	v_min_u32_dpp v127, v127, v127 row_ror:4 row_mask:0xf bank_mask:0xf
	v_add_f32_e32 v129, v129, v174
	v_add_f32_e32 v131, v131, v175
	v_max3_f32 v114, v114, v90, v94
	v_min_u32_dpp v127, v127, v127 row_ror:8 row_mask:0xf bank_mask:0xf
	v_add_f32_e32 v129, v129, v131
	v_mad_u32_u24 v249, v127, 24, v107
	s_nop 0
	v_add_f32_dpp v129, v129, v129 row_ror:1 row_mask:0xf bank_mask:0xf
	v_max_f32_e32 v114, v114, v116
	global_load_dword v156, v249, s[92:93]
	v_add_f32_dpp v129, v129, v129 row_ror:2 row_mask:0xf bank_mask:0xf
	s_nop 1
	v_add_f32_dpp v129, v129, v129 row_ror:4 row_mask:0xf bank_mask:0xf
	v_max_f32_dpp v114, v114, v114 row_ror:1 row_mask:0xf bank_mask:0xf
	s_nop 0
	v_add_f32_dpp v129, v129, v129 row_ror:8 row_mask:0xf bank_mask:0xf
	v_rcp_f32_e32 v246, v129
	s_nop 0
	v_pk_mul_f32 v[160:161], v[246:247], v[160:161] op_sel_hi:[0,1]
	v_pk_mul_f32 v[162:163], v[246:247], v[162:163] op_sel_hi:[0,1]
	v_max_f32_dpp v114, v114, v114 row_ror:2 row_mask:0xf bank_mask:0xf
	global_store_dwordx4 v111, v[160:163], s[90:91] sc1
	v_pk_mul_f32 v[164:165], v[246:247], v[164:165] op_sel_hi:[0,1]
	v_pk_mul_f32 v[166:167], v[246:247], v[166:167] op_sel_hi:[0,1]
	v_max_f32_dpp v114, v114, v114 row_ror:4 row_mask:0xf bank_mask:0xf
	global_store_dwordx4 v111, v[164:167], s[90:91] offset:256 sc1
	v_pk_mul_f32 v[168:169], v[246:247], v[168:169] op_sel_hi:[0,1]
	v_pk_mul_f32 v[170:171], v[246:247], v[170:171] op_sel_hi:[0,1]
	global_store_dwordx4 v111, v[168:171], s[90:91] offset:512 sc1
	v_max_f32_dpp v114, v114, v114 row_ror:8 row_mask:0xf bank_mask:0xf
	v_pk_mul_f32 v[172:173], v[246:247], v[172:173] op_sel_hi:[0,1]
	v_pk_mul_f32 v[174:175], v[246:247], v[174:175] op_sel_hi:[0,1]
	global_store_dwordx4 v111, v[172:175], s[90:91] offset:768 sc1
	s_add_i32 s70, s70, 1
	s_cmp_lt_u32 s70, 16
	s_cbranch_scc1 .Lk3m_loop
